# variant D plus gate/up GEMM next-unit gather offsets: 4 rowidx loads issued together with one wait instead of 4 load-wait steps
# baseline (speedup 1.0000x reference)
.LBB0_780:
	v_cndmask_b32_e64 v0, 0, 1, s[38:39]
	v_cmp_ne_u32_e64 s[2:3], 1, v0
	s_andn2_b64 vcc, exec, s[38:39]
	v_mov_b32_e32 v158, v140
	v_mov_b32_e32 v155, v134
	v_mov_b32_e32 v156, v136
	v_mov_b32_e32 v157, v138
	s_cbranch_vccnz .LBB0_790
	v_add_u32_e32 v200, s62, v146
	v_ashrrev_i32_e32 v201, 31, v200
	v_lshl_add_u64 v[200:201], v[200:201], 2, s[8:9]
	v_add_u32_e32 v202, s62, v147
	v_ashrrev_i32_e32 v203, 31, v202
	v_lshl_add_u64 v[202:203], v[202:203], 2, s[8:9]
	v_add_u32_e32 v204, s62, v148
	v_ashrrev_i32_e32 v205, 31, v204
	v_lshl_add_u64 v[204:205], v[204:205], 2, s[8:9]
	v_add_u32_e32 v206, s62, v149
	v_ashrrev_i32_e32 v207, 31, v206
	v_lshl_add_u64 v[206:207], v[206:207], 2, s[8:9]
	global_load_dword v208, v[200:201], off
	global_load_dword v209, v[202:203], off
	global_load_dword v210, v[204:205], off
	global_load_dword v211, v[206:207], off
	s_waitcnt vmcnt(0)
	v_lshlrev_b32_e32 v208, 10, v208
	v_lshlrev_b32_e32 v209, 10, v209
	v_lshlrev_b32_e32 v210, 10, v210
	v_lshlrev_b32_e32 v211, 10, v211
	v_and_b32_e32 v208, 0x3fff800, v208
	v_and_b32_e32 v209, 0x3fff800, v209
	v_and_b32_e32 v210, 0x3fff800, v210
	v_and_b32_e32 v211, 0x3fff800, v211
	v_cmp_gt_i32_e32 vcc, s63, v146
	s_nop 1
	v_cndmask_b32_e32 v0, 0, v208, vcc
	v_cmp_gt_i32_e32 vcc, s63, v147
	s_nop 1
	v_cndmask_b32_e32 v1, 0, v209, vcc
	v_cmp_gt_i32_e32 vcc, s63, v148
	s_nop 1
	v_cndmask_b32_e32 v3, 0, v210, vcc
	v_cmp_gt_i32_e32 vcc, s63, v149
	s_nop 1
	v_cndmask_b32_e32 v2, 0, v211, vcc
.LBB0_789:
	v_or_b32_e32 v155, v3, v150
	v_or_b32_e32 v156, v1, v150
	v_or_b32_e32 v157, v0, v150
	v_or_b32_e32 v158, v2, v150

.LBB0_4344:
	v_cndmask_b32_e64 v0, 0, 1, s[38:39]
	v_cmp_ne_u32_e64 s[2:3], 1, v0
	s_andn2_b64 vcc, exec, s[38:39]
	v_mov_b32_e32 v158, v140
	v_mov_b32_e32 v155, v134
	v_mov_b32_e32 v156, v136
	v_mov_b32_e32 v157, v138
	s_cbranch_vccnz .LBB0_4354
	v_add_u32_e32 v200, s61, v146
	v_ashrrev_i32_e32 v201, 31, v200
	v_lshl_add_u64 v[200:201], v[200:201], 2, s[8:9]
	v_add_u32_e32 v202, s61, v147
	v_ashrrev_i32_e32 v203, 31, v202
	v_lshl_add_u64 v[202:203], v[202:203], 2, s[8:9]
	v_add_u32_e32 v204, s61, v148
	v_ashrrev_i32_e32 v205, 31, v204
	v_lshl_add_u64 v[204:205], v[204:205], 2, s[8:9]
	v_add_u32_e32 v206, s61, v149
	v_ashrrev_i32_e32 v207, 31, v206
	v_lshl_add_u64 v[206:207], v[206:207], 2, s[8:9]
	global_load_dword v208, v[200:201], off
	global_load_dword v209, v[202:203], off
	global_load_dword v210, v[204:205], off
	global_load_dword v211, v[206:207], off
	s_waitcnt vmcnt(0)
	v_lshlrev_b32_e32 v208, 10, v208
	v_lshlrev_b32_e32 v209, 10, v209
	v_lshlrev_b32_e32 v210, 10, v210
	v_lshlrev_b32_e32 v211, 10, v211
	v_and_b32_e32 v208, 0x3fff800, v208
	v_and_b32_e32 v209, 0x3fff800, v209
	v_and_b32_e32 v210, 0x3fff800, v210
	v_and_b32_e32 v211, 0x3fff800, v211
	v_cmp_gt_i32_e32 vcc, s62, v146
	s_nop 1
	v_cndmask_b32_e32 v0, 0, v208, vcc
	v_cmp_gt_i32_e32 vcc, s62, v147
	s_nop 1
	v_cndmask_b32_e32 v1, 0, v209, vcc
	v_cmp_gt_i32_e32 vcc, s62, v148
	s_nop 1
	v_cndmask_b32_e32 v3, 0, v210, vcc
	v_cmp_gt_i32_e32 vcc, s62, v149
	s_nop 1
	v_cndmask_b32_e32 v2, 0, v211, vcc
